# speedup vs baseline: 1.0173x; 1.0106x over previous
.LBB2_53:
	s_lshl_b32 s2, s41, 14
	s_waitcnt lgkmcnt(0)
	s_add_u32 s2, s26, s2
	s_addc_u32 s3, s27, 0
	s_add_u32 s4, s2, 0x1000
	s_addc_u32 s5, s3, 0
	s_add_u32 s6, s2, 0x2000
	s_addc_u32 s7, s3, 0
	s_add_u32 s8, s2, 0x3000
	s_addc_u32 s9, s3, 0
	v_lshlrev_b32_e32 v94, 4, v1
	v_lshlrev_b32_e32 v68, 4, v68
	v_lshl_or_b32 v94, s41, 8, v94
	global_load_dwordx4 v[86:89], v94, s[36:37] offset:0
	global_load_dwordx4 v[90:93], v94, s[24:25] offset:0
	global_load_dwordx4 v[2:5], v68, s[2:3]
	global_load_dwordx4 v[6:9], v68, s[2:3] offset:1024
	global_load_dwordx4 v[10:13], v68, s[2:3] offset:2048
	global_load_dwordx4 v[14:17], v68, s[2:3] offset:3072
	global_load_dwordx4 v[18:21], v68, s[4:5]
	global_load_dwordx4 v[22:25], v68, s[4:5] offset:1024
	global_load_dwordx4 v[26:29], v68, s[4:5] offset:2048
	global_load_dwordx4 v[30:33], v68, s[4:5] offset:3072
	global_load_dwordx4 v[34:37], v68, s[6:7]
	global_load_dwordx4 v[38:41], v68, s[6:7] offset:1024
	global_load_dwordx4 v[42:45], v68, s[6:7] offset:2048
	global_load_dwordx4 v[46:49], v68, s[6:7] offset:3072
	global_load_dwordx4 v[50:53], v68, s[8:9]
	global_load_dwordx4 v[54:57], v68, s[8:9] offset:1024
	global_load_dwordx4 v[58:61], v68, s[8:9] offset:2048
	global_load_dwordx4 v[62:65], v68, s[8:9] offset:3072
	v_mul_u32_u24_e32 v67, 0x410, v69
	v_and_b32_e32 v95, 48, v0
	s_lshl_b32 s8, s41, 8
	v_add3_u32 v67, s8, v67, v95
	s_lshl_b32 s4, s41, 7
	s_addk_i32 s4, 0x4100
	s_movk_i32 s5, 0x210
	v_lshlrev_b32_e32 v66, 3, v1
	v_add_u32_e32 v66, s4, v66
	v_mad_u32_u24 v66, v69, s5, v66
	s_mov_b32 s4, 0x3fb8aa3b
	s_mov_b32 s5, 0x3fb8aa3b
	s_mov_b32 s8, -1.0
	s_mov_b32 s9, -1.0
	s_lshl_b32 s2, s41, 13
	s_add_u32 s2, s16, s2
	s_addc_u32 s3, s17, 0
	s_add_u32 s6, s2, 0x1000
	s_addc_u32 s7, s3, 0
	s_barrier
	ds_read_b128 v[70:73], v67
	ds_read_b128 v[74:77], v67 offset:64
	ds_read_b128 v[78:81], v67 offset:128
	ds_read_b128 v[82:85], v67 offset:192
	s_waitcnt vmcnt(15) lgkmcnt(3)
	v_mfma_f32_16x16x32_f16 v[2:5], v[2:5], v[70:73], 0
	s_waitcnt vmcnt(14) lgkmcnt(2)
	v_mfma_f32_16x16x32_f16 v[2:5], v[6:9], v[74:77], v[2:5]
	s_waitcnt vmcnt(13) lgkmcnt(1)
	v_mfma_f32_16x16x32_f16 v[2:5], v[10:13], v[78:81], v[2:5]
	s_waitcnt vmcnt(12) lgkmcnt(0)
	v_mfma_f32_16x16x32_f16 v[2:5], v[14:17], v[82:85], v[2:5]
	s_load_dwordx2 s[46:47], s[0:1], 0x50
	s_load_dwordx4 s[48:51], s[0:1], 0x58
	global_load_dwordx4 v[6:9], v94, s[36:37] offset:64
	global_load_dwordx4 v[10:13], v94, s[24:25] offset:64
	s_waitcnt vmcnt(13)
	v_mfma_f32_16x16x32_f16 v[18:21], v[18:21], v[70:73], 0
	s_waitcnt vmcnt(12)
	v_mfma_f32_16x16x32_f16 v[18:21], v[22:25], v[74:77], v[18:21]
	s_waitcnt vmcnt(11)
	v_mfma_f32_16x16x32_f16 v[18:21], v[26:29], v[78:81], v[18:21]
	s_waitcnt vmcnt(10)
	v_mfma_f32_16x16x32_f16 v[18:21], v[30:33], v[82:85], v[18:21]
	global_load_dwordx4 v[22:25], v94, s[36:37] offset:128
	global_load_dwordx4 v[26:29], v94, s[24:25] offset:128
	v_pk_add_f32 v[2:3], v[2:3], v[86:87]
	v_pk_add_f32 v[4:5], v[4:5], v[88:89]
	v_pk_mul_f32 v[14:15], v[2:3], s[4:5]
	v_pk_mul_f32 v[16:17], v[4:5], s[4:5]
	v_exp_f32_e32 v14, v14
	v_exp_f32_e32 v15, v15
	v_exp_f32_e32 v16, v16
	v_exp_f32_e32 v17, v17
	v_cmp_lt_f32_e64 s[10:11], 0, v2
	v_cmp_lt_f32_e64 s[12:13], 0, v3
	v_cmp_lt_f32_e64 s[20:21], 0, v4
	v_cmp_lt_f32_e64 s[22:23], 0, v5
	v_pk_add_f32 v[14:15], v[14:15], s[8:9]
	v_pk_add_f32 v[16:17], v[16:17], s[8:9]
	v_cndmask_b32_e64 v2, v14, v2, s[10:11]
	v_cndmask_b32_e64 v3, v15, v3, s[12:13]
	v_cndmask_b32_e64 v4, v16, v4, s[20:21]
	v_cndmask_b32_e64 v5, v17, v5, s[22:23]
	v_pk_add_f32 v[2:3], v[2:3], v[90:91] neg_lo:[0,1] neg_hi:[0,1]
	v_pk_add_f32 v[4:5], v[4:5], v[92:93] neg_lo:[0,1] neg_hi:[0,1]
	v_cvt_pk_f16_f32 v14, v2, v3
	v_cvt_pk_f16_f32 v15, v4, v5
	ds_write_b64 v66, v[14:15] offset:0
	s_waitcnt vmcnt(11)
	v_mfma_f32_16x16x32_f16 v[34:37], v[34:37], v[70:73], 0
	s_waitcnt vmcnt(10)
	v_mfma_f32_16x16x32_f16 v[34:37], v[38:41], v[74:77], v[34:37]
	s_waitcnt vmcnt(9)
	v_mfma_f32_16x16x32_f16 v[34:37], v[42:45], v[78:81], v[34:37]
	s_waitcnt vmcnt(8)
	v_mfma_f32_16x16x32_f16 v[34:37], v[46:49], v[82:85], v[34:37]
	global_load_dwordx4 v[38:41], v94, s[36:37] offset:192
	global_load_dwordx4 v[42:45], v94, s[24:25] offset:192
	s_waitcnt vmcnt(9)
	v_mfma_f32_16x16x32_f16 v[50:53], v[50:53], v[70:73], 0
	s_waitcnt vmcnt(8)
	v_mfma_f32_16x16x32_f16 v[50:53], v[54:57], v[74:77], v[50:53]
	s_waitcnt vmcnt(7)
	v_mfma_f32_16x16x32_f16 v[50:53], v[58:61], v[78:81], v[50:53]
	s_waitcnt vmcnt(6)
	v_mfma_f32_16x16x32_f16 v[50:53], v[62:65], v[82:85], v[50:53]
	s_waitcnt vmcnt(4)
	v_pk_add_f32 v[18:19], v[18:19], v[6:7]
	v_pk_add_f32 v[20:21], v[20:21], v[8:9]
	v_pk_mul_f32 v[14:15], v[18:19], s[4:5]
	v_pk_mul_f32 v[16:17], v[20:21], s[4:5]
	v_exp_f32_e32 v14, v14
	v_exp_f32_e32 v15, v15
	v_exp_f32_e32 v16, v16
	v_exp_f32_e32 v17, v17
	v_cmp_lt_f32_e64 s[10:11], 0, v18
	v_cmp_lt_f32_e64 s[12:13], 0, v19
	v_cmp_lt_f32_e64 s[20:21], 0, v20
	v_cmp_lt_f32_e64 s[22:23], 0, v21
	v_pk_add_f32 v[14:15], v[14:15], s[8:9]
	v_pk_add_f32 v[16:17], v[16:17], s[8:9]
	v_cndmask_b32_e64 v18, v14, v18, s[10:11]
	v_cndmask_b32_e64 v19, v15, v19, s[12:13]
	v_cndmask_b32_e64 v20, v16, v20, s[20:21]
	v_cndmask_b32_e64 v21, v17, v21, s[22:23]
	v_pk_add_f32 v[18:19], v[18:19], v[10:11] neg_lo:[0,1] neg_hi:[0,1]
	v_pk_add_f32 v[20:21], v[20:21], v[12:13] neg_lo:[0,1] neg_hi:[0,1]
	v_cvt_pk_f16_f32 v14, v18, v19
	v_cvt_pk_f16_f32 v15, v20, v21
	ds_write_b64 v66, v[14:15] offset:32
	global_load_dwordx4 v[2:5], v68, s[2:3]
	global_load_dwordx4 v[6:9], v68, s[2:3] offset:1024
	global_load_dwordx4 v[10:13], v68, s[2:3] offset:2048
	global_load_dwordx4 v[14:17], v68, s[2:3] offset:3072
	global_load_dwordx4 v[18:21], v68, s[6:7]
	s_waitcnt vmcnt(7)
	v_pk_add_f32 v[34:35], v[34:35], v[22:23]
	v_pk_add_f32 v[36:37], v[36:37], v[24:25]
	v_pk_mul_f32 v[46:47], v[34:35], s[4:5]
	v_pk_mul_f32 v[48:49], v[36:37], s[4:5]
	v_exp_f32_e32 v46, v46
	v_exp_f32_e32 v47, v47
	v_exp_f32_e32 v48, v48
	v_exp_f32_e32 v49, v49
	v_cmp_lt_f32_e64 s[10:11], 0, v34
	v_cmp_lt_f32_e64 s[12:13], 0, v35
	v_cmp_lt_f32_e64 s[20:21], 0, v36
	v_cmp_lt_f32_e64 s[22:23], 0, v37
	v_pk_add_f32 v[46:47], v[46:47], s[8:9]
	v_pk_add_f32 v[48:49], v[48:49], s[8:9]
	v_cndmask_b32_e64 v34, v46, v34, s[10:11]
	v_cndmask_b32_e64 v35, v47, v35, s[12:13]
	v_cndmask_b32_e64 v36, v48, v36, s[20:21]
	v_cndmask_b32_e64 v37, v49, v37, s[22:23]
	v_pk_add_f32 v[34:35], v[34:35], v[26:27] neg_lo:[0,1] neg_hi:[0,1]
	v_pk_add_f32 v[36:37], v[36:37], v[28:29] neg_lo:[0,1] neg_hi:[0,1]
	v_cvt_pk_f16_f32 v46, v34, v35
	v_cvt_pk_f16_f32 v47, v36, v37
	ds_write_b64 v66, v[46:47] offset:64
	global_load_dwordx4 v[22:25], v68, s[6:7] offset:1024
	global_load_dwordx4 v[26:29], v68, s[6:7] offset:2048
	global_load_dwordx4 v[30:33], v68, s[6:7] offset:3072
	s_waitcnt vmcnt(8)
	v_pk_add_f32 v[50:51], v[50:51], v[38:39]
	v_pk_add_f32 v[52:53], v[52:53], v[40:41]
	v_pk_mul_f32 v[46:47], v[50:51], s[4:5]
	v_pk_mul_f32 v[48:49], v[52:53], s[4:5]
	v_exp_f32_e32 v46, v46
	v_exp_f32_e32 v47, v47
	v_exp_f32_e32 v48, v48
	v_exp_f32_e32 v49, v49
	v_cmp_lt_f32_e64 s[10:11], 0, v50
	v_cmp_lt_f32_e64 s[12:13], 0, v51
	v_cmp_lt_f32_e64 s[20:21], 0, v52
	v_cmp_lt_f32_e64 s[22:23], 0, v53
	v_pk_add_f32 v[46:47], v[46:47], s[8:9]
	v_pk_add_f32 v[48:49], v[48:49], s[8:9]
	v_cndmask_b32_e64 v50, v46, v50, s[10:11]
	v_cndmask_b32_e64 v51, v47, v51, s[12:13]
	v_cndmask_b32_e64 v52, v48, v52, s[20:21]
	v_cndmask_b32_e64 v53, v49, v53, s[22:23]
	v_pk_add_f32 v[50:51], v[50:51], v[42:43] neg_lo:[0,1] neg_hi:[0,1]
	v_pk_add_f32 v[52:53], v[52:53], v[44:45] neg_lo:[0,1] neg_hi:[0,1]
	v_cvt_pk_f16_f32 v46, v50, v51
	v_cvt_pk_f16_f32 v47, v52, v53
	ds_write_b64 v66, v[46:47] offset:96
	v_mul_u32_u24_e32 v35, 0x210, v69
	v_lshl_or_b32 v34, v1, 2, 1
	v_add_u32_e32 v35, v35, v95
	s_waitcnt lgkmcnt(0)
	s_barrier
	ds_read_b128 v[36:39], v35 offset:16640
	ds_read_b128 v[40:43], v35 offset:16704
	s_movk_i32 s2, 0x440
	s_waitcnt vmcnt(7) lgkmcnt(1)
	v_mfma_f32_16x16x32_f16 v[2:5], v[36:39], v[2:5], 0
	ds_read_b128 v[36:39], v35 offset:16768
	s_waitcnt vmcnt(6) lgkmcnt(1)
	v_mfma_f32_16x16x32_f16 v[2:5], v[40:43], v[6:9], v[2:5]
	ds_read_b128 v[6:9], v35 offset:16832
	s_waitcnt vmcnt(5) lgkmcnt(1)
	v_mfma_f32_16x16x32_f16 v[2:5], v[36:39], v[10:13], v[2:5]
	ds_read_b128 v[10:13], v35 offset:16896
	s_waitcnt vmcnt(4) lgkmcnt(1)
	v_mfma_f32_16x16x32_f16 v[2:5], v[6:9], v[14:17], v[2:5]
	ds_read_b128 v[6:9], v35 offset:16960
	s_waitcnt vmcnt(3) lgkmcnt(1)
	v_mfma_f32_16x16x32_f16 v[2:5], v[10:13], v[18:21], v[2:5]
	ds_read_b128 v[10:13], v35 offset:17024
	s_waitcnt vmcnt(2) lgkmcnt(1)
	v_mfma_f32_16x16x32_f16 v[2:5], v[6:9], v[22:25], v[2:5]
	ds_read_b128 v[6:9], v35 offset:17088
	s_waitcnt vmcnt(1) lgkmcnt(1)
	v_mfma_f32_16x16x32_f16 v[2:5], v[10:13], v[26:29], v[2:5]
	s_waitcnt vmcnt(0) lgkmcnt(0)
	v_mfma_f32_16x16x32_f16 v[2:5], v[6:9], v[30:33], v[2:5]
	v_lshlrev_b32_e32 v6, 2, v69
	v_lshl_or_b32 v7, s41, 6, v6
	v_mad_u32_u24 v1, v1, s2, v7
	s_movk_i32 s2, 0x110
	s_nop 3
	ds_write_b32 v1, v2
	v_mad_u32_u24 v1, v34, s2, v7
	v_lshlrev_b32_e32 v2, 4, v69
	ds_write2_b32 v1, v3, v4 offset1:68
	ds_write_b32 v1, v5 offset:544
	s_waitcnt lgkmcnt(0)
	global_load_dwordx4 v[8:11], v2, s[24:25] offset:1024
	global_load_dwordx4 v[12:15], v2, s[18:19]
	global_load_dwordx4 v[16:19], v2, s[14:15]
	v_lshrrev_b32_e32 v1, 4, v0
	v_mad_u32_u24 v2, v1, s2, v2
	s_barrier
	ds_read_b128 v[2:5], v2
	s_movk_i32 s2, 0x100
	s_waitcnt vmcnt(2) lgkmcnt(0)
	v_add_f32_e32 v9, v3, v9
	v_add_f32_e32 v8, v2, v8
	s_waitcnt vmcnt(1)
	v_mul_f32_e32 v13, v13, v9
	s_waitcnt vmcnt(0)
	v_mul_f32_e32 v9, v17, v9
	v_add_f32_e32 v10, v4, v10
	v_fmac_f32_e32 v13, v12, v8
	v_fmac_f32_e32 v9, v16, v8
	v_add_f32_e32 v11, v5, v11
	v_fmac_f32_e32 v13, v14, v10
	v_fmac_f32_e32 v9, v18, v10
	v_fmac_f32_e32 v13, v15, v11
	v_fmac_f32_e32 v9, v19, v11
	s_nop 1
	v_add_f32_dpp v13, v13, v13 row_mirror row_mask:0xf bank_mask:0xf
	v_add_f32_dpp v9, v9, v9 row_mirror row_mask:0xf bank_mask:0xf
	s_nop 0
	v_add_f32_dpp v13, v13, v13 row_half_mirror row_mask:0xf bank_mask:0xf
	v_add_f32_dpp v9, v9, v9 row_half_mirror row_mask:0xf bank_mask:0xf
	s_nop 0
	v_add_f32_dpp v13, v13, v13 quad_perm:[2,3,0,1] row_mask:0xf bank_mask:0xf
	v_add_f32_dpp v9, v9, v9 quad_perm:[2,3,0,1] row_mask:0xf bank_mask:0xf
	s_nop 0
	v_add_f32_dpp v7, v13, v13 quad_perm:[1,0,3,2] row_mask:0xf bank_mask:0xf
	v_add_f32_dpp v12, v9, v9 quad_perm:[1,0,3,2] row_mask:0xf bank_mask:0xf
	v_cmp_gt_u32_e32 vcc, s2, v0
	s_and_saveexec_b64 s[2:3], vcc
	s_cbranch_execz .LBB2_57
	v_lshlrev_b32_e32 v0, 2, v1
	ds_read_b32 v0, v0 offset:25152
	v_cmp_eq_u32_e32 vcc, 0, v69
	s_waitcnt lgkmcnt(0)
	v_add_u32_e32 v0, s33, v0
	v_ashrrev_i32_e32 v1, 31, v0
	s_and_saveexec_b64 s[4:5], vcc
	s_cbranch_execz .LBB2_56
	v_lshlrev_b64 v[8:9], 2, v[0:1]
	v_lshl_add_u64 v[10:11], s[50:51], 0, v[8:9]
	v_lshl_add_u64 v[8:9], s[48:49], 0, v[8:9]
	global_store_dword v[8:9], v7, off
	global_store_dword v[10:11], v12, off
.LBB2_56:
	s_or_b64 exec, exec, s[4:5]
	v_cvt_f16_f32_e32 v2, v2
	v_cvt_f16_f32_e32 v5, v5
	v_cvt_pk_f16_f32 v3, v3, v4
	v_lshlrev_b64 v[0:1], 7, v[0:1]
	v_pack_b32_f16 v2, v2, v3
	v_alignbit_b32 v3, v5, v3, 16
	v_lshl_add_u64 v[0:1], s[46:47], 0, v[0:1]
	v_lshlrev_b32_e32 v4, 1, v6
	v_mov_b32_e32 v5, 0
	v_lshl_add_u64 v[0:1], v[0:1], 0, v[4:5]
	global_store_dwordx2 v[0:1], v[2:3], off
.LBB2_57:
	s_endpgm
	s_nop 0
	s_nop 0
	s_nop 0
	s_nop 0
	s_nop 0
	s_nop 0
	s_nop 0
	s_nop 0
	s_nop 0
	s_nop 0
	s_nop 0
	s_nop 0
	s_nop 0
	s_nop 0
	s_nop 0
	s_endpgm
